# selection pass 1 stops after the last key register the row actually uses (rows shorter than 8192 keys skip the all-zero registers)
# speedup vs baseline: 1.0049x; 1.0049x over previous
; #define LAS __attribute__((address_space(3)))
; __device__ __forceinline__ bool dsa2_sampled(LAS unsigned char* wl, const unsigned (&kk)[128], int nreg, int n, int lane) {
;     ...
;     bl = bl < 1u ? 1u : bl; if (bl > bh) bl = bh;
;     int cur = 0; LAS unsigned* pp = (LAS unsigned*)(PRIV + lane);
; #pragma unroll
;     for (int i = 0; i < 128; ++i) { if ((i & ~15) < nreg) { const unsigned k = kk[i];
;             if ((k >> 21) >= bl) { if (cur < 24) { pp[0] = (unsigned)(lane + 64 * i); pp[1] = k; } pp += 128; ++cur; } }
;         __builtin_amdgcn_sched_barrier(0); }
.LBB0_763:
	s_waitcnt lgkmcnt(0)
	v_min_u32_e32 v0, v168, v2
	v_lshl_add_u32 v6, v129, 3, s57
	s_mov_b64 s[0:1], exec
	v_lshlrev_b32_e32 v0, 21, v0
	v_mov_b32_e32 v1, v6
	v_add_u32_e32 v5, 0x2e00, v6
	v_cmp_ge_u32_e32 vcc, v166, v0
	s_mov_b64 exec, vcc
	ds_write2_b32 v1, v129, v166 offset1:1
	v_add_u32_e32 v1, 0x200, v1
	s_mov_b64 exec, s[0:1]
	v_cmp_ge_u32_e32 vcc, v165, v0
	v_or_b32_e32 v4, 0x40, v129
	s_mov_b64 exec, vcc
	ds_write2_b32 v1, v4, v165 offset1:1
	v_add_u32_e32 v1, 0x200, v1
	s_mov_b64 exec, s[0:1]
	v_cmp_ge_u32_e32 vcc, v164, v0
	v_or_b32_e32 v4, 0x80, v129
	s_mov_b64 exec, vcc
	ds_write2_b32 v1, v4, v164 offset1:1
	v_add_u32_e32 v1, 0x200, v1
	s_mov_b64 exec, s[0:1]
	v_cmp_ge_u32_e32 vcc, v163, v0
	v_or_b32_e32 v4, 0xc0, v129
	s_mov_b64 exec, vcc
	ds_write2_b32 v1, v4, v163 offset1:1
	v_add_u32_e32 v1, 0x200, v1
	s_mov_b64 exec, s[0:1]
	v_cmp_ge_u32_e32 vcc, v162, v0
	v_or_b32_e32 v4, 0x100, v129
	s_mov_b64 exec, vcc
	ds_write2_b32 v1, v4, v162 offset1:1
	v_add_u32_e32 v1, 0x200, v1
	s_mov_b64 exec, s[0:1]
	v_cmp_ge_u32_e32 vcc, v161, v0
	v_or_b32_e32 v4, 0x140, v129
	s_mov_b64 exec, vcc
	ds_write2_b32 v1, v4, v161 offset1:1
	v_add_u32_e32 v1, 0x200, v1
	s_mov_b64 exec, s[0:1]
	v_cmp_ge_u32_e32 vcc, v160, v0
	v_or_b32_e32 v4, 0x180, v129
	s_mov_b64 exec, vcc
	ds_write2_b32 v1, v4, v160 offset1:1
	v_add_u32_e32 v1, 0x200, v1
	s_mov_b64 exec, s[0:1]
	v_cmp_ge_u32_e32 vcc, v159, v0
	v_or_b32_e32 v4, 0x1c0, v129
	s_mov_b64 exec, vcc
	ds_write2_b32 v1, v4, v159 offset1:1
	v_add_u32_e32 v1, 0x200, v1
	s_mov_b64 exec, s[0:1]
	v_cmp_ge_u32_e32 vcc, v158, v0
	v_or_b32_e32 v4, 0x200, v129
	s_mov_b64 exec, vcc
	ds_write2_b32 v1, v4, v158 offset1:1
	v_add_u32_e32 v1, 0x200, v1
	s_mov_b64 exec, s[0:1]
	v_cmp_ge_u32_e32 vcc, v157, v0
	v_or_b32_e32 v4, 0x240, v129
	s_mov_b64 exec, vcc
	ds_write2_b32 v1, v4, v157 offset1:1
	v_add_u32_e32 v1, 0x200, v1
	s_mov_b64 exec, s[0:1]
	v_cmp_ge_u32_e32 vcc, v155, v0
	v_or_b32_e32 v4, 0x280, v129
	s_mov_b64 exec, vcc
	ds_write2_b32 v1, v4, v155 offset1:1
	v_add_u32_e32 v1, 0x200, v1
	s_mov_b64 exec, s[0:1]
	v_cmp_ge_u32_e32 vcc, v154, v0
	v_or_b32_e32 v4, 0x2c0, v129
	s_mov_b64 exec, vcc
	ds_write2_b32 v1, v4, v154 offset1:1
	v_add_u32_e32 v1, 0x200, v1
	s_mov_b64 exec, s[0:1]
	v_cmp_ge_u32_e32 vcc, v153, v0
	v_or_b32_e32 v4, 0x300, v129
	s_mov_b64 exec, vcc
	ds_write2_b32 v1, v4, v153 offset1:1
	v_add_u32_e32 v1, 0x200, v1
	s_mov_b64 exec, s[0:1]
	v_cmp_ge_u32_e32 vcc, v152, v0
	v_or_b32_e32 v4, 0x340, v129
	s_mov_b64 exec, vcc
	ds_write2_b32 v1, v4, v152 offset1:1
	v_add_u32_e32 v1, 0x200, v1
	s_mov_b64 exec, s[0:1]
	v_cmp_ge_u32_e32 vcc, v151, v0
	v_or_b32_e32 v4, 0x380, v129
	s_mov_b64 exec, vcc
	ds_write2_b32 v1, v4, v151 offset1:1
	v_add_u32_e32 v1, 0x200, v1
	s_mov_b64 exec, s[0:1]
	v_cmp_ge_u32_e32 vcc, v149, v0
	v_or_b32_e32 v4, 0x3c0, v129
	s_mov_b64 exec, vcc
	ds_write2_b32 v1, v4, v149 offset1:1
	v_add_u32_e32 v1, 0x200, v1
	s_mov_b64 exec, s[0:1]
	v_cmp_ge_u32_e32 vcc, v148, v0
	v_or_b32_e32 v4, 0x400, v129
	s_mov_b64 exec, vcc
	ds_write2_b32 v1, v4, v148 offset1:1
	v_add_u32_e32 v1, 0x200, v1
	s_mov_b64 exec, s[0:1]
	v_cmp_ge_u32_e32 vcc, v147, v0
	v_or_b32_e32 v4, 0x440, v129
	s_mov_b64 exec, vcc
	ds_write2_b32 v1, v4, v147 offset1:1
	v_add_u32_e32 v1, 0x200, v1
	s_mov_b64 exec, s[0:1]
	v_cmp_ge_u32_e32 vcc, v146, v0
	v_or_b32_e32 v4, 0x480, v129
	s_mov_b64 exec, vcc
	ds_write2_b32 v1, v4, v146 offset1:1
	v_add_u32_e32 v1, 0x200, v1
	s_mov_b64 exec, s[0:1]
	v_cmp_ge_u32_e32 vcc, v145, v0
	v_or_b32_e32 v4, 0x4c0, v129
	s_mov_b64 exec, vcc
	ds_write2_b32 v1, v4, v145 offset1:1
	v_add_u32_e32 v1, 0x200, v1
	s_mov_b64 exec, s[0:1]
	v_cmp_ge_u32_e32 vcc, v144, v0
	v_or_b32_e32 v4, 0x500, v129
	s_mov_b64 exec, vcc
	ds_write2_b32 v1, v4, v144 offset1:1
	v_add_u32_e32 v1, 0x200, v1
	s_mov_b64 exec, s[0:1]
	v_cmp_ge_u32_e32 vcc, v143, v0
	v_or_b32_e32 v4, 0x540, v129
	s_mov_b64 exec, vcc
	ds_write2_b32 v1, v4, v143 offset1:1
	v_add_u32_e32 v1, 0x200, v1
	s_mov_b64 exec, s[0:1]
	v_cmp_ge_u32_e32 vcc, v142, v0
	v_or_b32_e32 v4, 0x580, v129
	s_mov_b64 exec, vcc
	ds_write2_b32 v1, v4, v142 offset1:1
	v_add_u32_e32 v1, 0x200, v1
	s_mov_b64 exec, s[0:1]
	v_cmp_ge_u32_e32 vcc, v141, v0
	v_or_b32_e32 v4, 0x5c0, v129
	s_mov_b64 exec, vcc
	ds_write2_b32 v1, v4, v141 offset1:1
	v_add_u32_e32 v1, 0x200, v1
	s_mov_b64 exec, s[0:1]
	s_cmpk_le_u32 s49, 0x18
	s_cbranch_scc1 .Lp1_done
	v_cmp_ge_u32_e32 vcc, v140, v0
	v_or_b32_e32 v4, 0x600, v129
	v_min_u32_e32 v3, v1, v5
	s_mov_b64 exec, vcc
	ds_write2_b32 v3, v4, v140 offset1:1
	v_add_u32_e32 v1, 0x200, v1
	s_mov_b64 exec, s[0:1]
	v_cmp_ge_u32_e32 vcc, v139, v0
	v_or_b32_e32 v4, 0x640, v129
	v_min_u32_e32 v3, v1, v5
	s_mov_b64 exec, vcc
	ds_write2_b32 v3, v4, v139 offset1:1
	v_add_u32_e32 v1, 0x200, v1
	s_mov_b64 exec, s[0:1]
	v_cmp_ge_u32_e32 vcc, v137, v0
	v_or_b32_e32 v4, 0x680, v129
	v_min_u32_e32 v3, v1, v5
	s_mov_b64 exec, vcc
	ds_write2_b32 v3, v4, v137 offset1:1
	v_add_u32_e32 v1, 0x200, v1
	s_mov_b64 exec, s[0:1]
	v_cmp_ge_u32_e32 vcc, v136, v0
	v_or_b32_e32 v4, 0x6c0, v129
	v_min_u32_e32 v3, v1, v5
	s_mov_b64 exec, vcc
	ds_write2_b32 v3, v4, v136 offset1:1
	v_add_u32_e32 v1, 0x200, v1
	s_mov_b64 exec, s[0:1]
	v_cmp_ge_u32_e32 vcc, v134, v0
	v_or_b32_e32 v4, 0x700, v129
	v_min_u32_e32 v3, v1, v5
	s_mov_b64 exec, vcc
	ds_write2_b32 v3, v4, v134 offset1:1
	v_add_u32_e32 v1, 0x200, v1
	s_mov_b64 exec, s[0:1]
	v_cmp_ge_u32_e32 vcc, v132, v0
	v_or_b32_e32 v4, 0x740, v129
	v_min_u32_e32 v3, v1, v5
	s_mov_b64 exec, vcc
	ds_write2_b32 v3, v4, v132 offset1:1
	v_add_u32_e32 v1, 0x200, v1
	s_mov_b64 exec, s[0:1]
	v_cmp_ge_u32_e32 vcc, v130, v0
	v_or_b32_e32 v4, 0x780, v129
	v_min_u32_e32 v3, v1, v5
	s_mov_b64 exec, vcc
	ds_write2_b32 v3, v4, v130 offset1:1
	v_add_u32_e32 v1, 0x200, v1
	s_mov_b64 exec, s[0:1]
	v_cmp_ge_u32_e32 vcc, v126, v0
	v_or_b32_e32 v4, 0x7c0, v129
	v_min_u32_e32 v3, v1, v5
	s_mov_b64 exec, vcc
	ds_write2_b32 v3, v4, v126 offset1:1
	v_add_u32_e32 v1, 0x200, v1
	s_mov_b64 exec, s[0:1]
	s_cmpk_le_u32 s49, 0x20
	s_cbranch_scc1 .Lp1_done
; #define LAS __attribute__((address_space(3)))
; __device__ __forceinline__ bool dsa2_sampled(LAS unsigned char* wl, const unsigned (&kk)[128], int nreg, int n, int lane) {
;     ...
;     bl = bl < 1u ? 1u : bl; if (bl > bh) bl = bh;
;     int cur = 0; LAS unsigned* pp = (LAS unsigned*)(PRIV + lane);
; #pragma unroll
;     for (int i = 0; i < 128; ++i) { if ((i & ~15) < nreg) { const unsigned k = kk[i];
;             if ((k >> 21) >= bl) { if (cur < 24) { pp[0] = (unsigned)(lane + 64 * i); pp[1] = k; } pp += 128; ++cur; } }
;         __builtin_amdgcn_sched_barrier(0); }
	v_cmp_ge_u32_e32 vcc, v135, v0
	v_or_b32_e32 v4, 0x800, v129
	v_min_u32_e32 v3, v1, v5
	s_mov_b64 exec, vcc
	ds_write2_b32 v3, v4, v135 offset1:1
	v_add_u32_e32 v1, 0x200, v1
	s_mov_b64 exec, s[0:1]
	v_cmp_ge_u32_e32 vcc, v133, v0
	v_or_b32_e32 v4, 0x840, v129
	v_min_u32_e32 v3, v1, v5
	s_mov_b64 exec, vcc
	ds_write2_b32 v3, v4, v133 offset1:1
	v_add_u32_e32 v1, 0x200, v1
	s_mov_b64 exec, s[0:1]
	v_cmp_ge_u32_e32 vcc, v131, v0
	v_or_b32_e32 v4, 0x880, v129
	v_min_u32_e32 v3, v1, v5
	s_mov_b64 exec, vcc
	ds_write2_b32 v3, v4, v131 offset1:1
	v_add_u32_e32 v1, 0x200, v1
	s_mov_b64 exec, s[0:1]
	v_cmp_ge_u32_e32 vcc, v127, v0
	v_or_b32_e32 v4, 0x8c0, v129
	v_min_u32_e32 v3, v1, v5
	s_mov_b64 exec, vcc
	ds_write2_b32 v3, v4, v127 offset1:1
	v_add_u32_e32 v1, 0x200, v1
	s_mov_b64 exec, s[0:1]
	v_cmp_ge_u32_e32 vcc, v125, v0
	v_or_b32_e32 v4, 0x900, v129
	v_min_u32_e32 v3, v1, v5
	s_mov_b64 exec, vcc
	ds_write2_b32 v3, v4, v125 offset1:1
	v_add_u32_e32 v1, 0x200, v1
	s_mov_b64 exec, s[0:1]
	v_cmp_ge_u32_e32 vcc, v124, v0
	v_or_b32_e32 v4, 0x940, v129
	v_min_u32_e32 v3, v1, v5
	s_mov_b64 exec, vcc
	ds_write2_b32 v3, v4, v124 offset1:1
	v_add_u32_e32 v1, 0x200, v1
	s_mov_b64 exec, s[0:1]
	v_cmp_ge_u32_e32 vcc, v123, v0
	v_or_b32_e32 v4, 0x980, v129
	v_min_u32_e32 v3, v1, v5
	s_mov_b64 exec, vcc
	ds_write2_b32 v3, v4, v123 offset1:1
	v_add_u32_e32 v1, 0x200, v1
	s_mov_b64 exec, s[0:1]
	v_cmp_ge_u32_e32 vcc, v122, v0
	v_or_b32_e32 v4, 0x9c0, v129
	v_min_u32_e32 v3, v1, v5
	s_mov_b64 exec, vcc
	ds_write2_b32 v3, v4, v122 offset1:1
	v_add_u32_e32 v1, 0x200, v1
	s_mov_b64 exec, s[0:1]
	s_cmpk_le_u32 s49, 0x28
	s_cbranch_scc1 .Lp1_done
	v_cmp_ge_u32_e32 vcc, v121, v0
	v_or_b32_e32 v4, 0xa00, v129
	v_min_u32_e32 v3, v1, v5
	s_mov_b64 exec, vcc
	ds_write2_b32 v3, v4, v121 offset1:1
	v_add_u32_e32 v1, 0x200, v1
	s_mov_b64 exec, s[0:1]
	v_cmp_ge_u32_e32 vcc, v120, v0
	v_or_b32_e32 v4, 0xa40, v129
	v_min_u32_e32 v3, v1, v5
	s_mov_b64 exec, vcc
	ds_write2_b32 v3, v4, v120 offset1:1
	v_add_u32_e32 v1, 0x200, v1
	s_mov_b64 exec, s[0:1]
	v_cmp_ge_u32_e32 vcc, v119, v0
	v_or_b32_e32 v4, 0xa80, v129
	v_min_u32_e32 v3, v1, v5
	s_mov_b64 exec, vcc
	ds_write2_b32 v3, v4, v119 offset1:1
	v_add_u32_e32 v1, 0x200, v1
	s_mov_b64 exec, s[0:1]
	v_cmp_ge_u32_e32 vcc, v118, v0
	v_or_b32_e32 v4, 0xac0, v129
	v_min_u32_e32 v3, v1, v5
	s_mov_b64 exec, vcc
	ds_write2_b32 v3, v4, v118 offset1:1
	v_add_u32_e32 v1, 0x200, v1
	s_mov_b64 exec, s[0:1]
	v_cmp_ge_u32_e32 vcc, v117, v0
	v_or_b32_e32 v4, 0xb00, v129
	v_min_u32_e32 v3, v1, v5
	s_mov_b64 exec, vcc
	ds_write2_b32 v3, v4, v117 offset1:1
	v_add_u32_e32 v1, 0x200, v1
	s_mov_b64 exec, s[0:1]
	v_cmp_ge_u32_e32 vcc, v116, v0
	v_or_b32_e32 v4, 0xb40, v129
	v_min_u32_e32 v3, v1, v5
	s_mov_b64 exec, vcc
	ds_write2_b32 v3, v4, v116 offset1:1
	v_add_u32_e32 v1, 0x200, v1
	s_mov_b64 exec, s[0:1]
	v_cmp_ge_u32_e32 vcc, v115, v0
	v_or_b32_e32 v4, 0xb80, v129
	v_min_u32_e32 v3, v1, v5
	s_mov_b64 exec, vcc
	ds_write2_b32 v3, v4, v115 offset1:1
	v_add_u32_e32 v1, 0x200, v1
	s_mov_b64 exec, s[0:1]
	v_cmp_ge_u32_e32 vcc, v114, v0
	v_or_b32_e32 v4, 0xbc0, v129
	v_min_u32_e32 v3, v1, v5
	s_mov_b64 exec, vcc
	ds_write2_b32 v3, v4, v114 offset1:1
	v_add_u32_e32 v1, 0x200, v1
	s_mov_b64 exec, s[0:1]
	s_cmpk_le_u32 s49, 0x30
	s_cbranch_scc1 .Lp1_done
	v_cmp_ge_u32_e32 vcc, v113, v0
	v_or_b32_e32 v4, 0xc00, v129
	v_min_u32_e32 v3, v1, v5
	s_mov_b64 exec, vcc
	ds_write2_b32 v3, v4, v113 offset1:1
	v_add_u32_e32 v1, 0x200, v1
	s_mov_b64 exec, s[0:1]
	v_cmp_ge_u32_e32 vcc, v112, v0
	v_or_b32_e32 v4, 0xc40, v129
	v_min_u32_e32 v3, v1, v5
	s_mov_b64 exec, vcc
	ds_write2_b32 v3, v4, v112 offset1:1
	v_add_u32_e32 v1, 0x200, v1
	s_mov_b64 exec, s[0:1]
	v_cmp_ge_u32_e32 vcc, v111, v0
	v_or_b32_e32 v4, 0xc80, v129
	v_min_u32_e32 v3, v1, v5
	s_mov_b64 exec, vcc
	ds_write2_b32 v3, v4, v111 offset1:1
	v_add_u32_e32 v1, 0x200, v1
	s_mov_b64 exec, s[0:1]
	v_cmp_ge_u32_e32 vcc, v110, v0
	v_or_b32_e32 v4, 0xcc0, v129
	v_min_u32_e32 v3, v1, v5
	s_mov_b64 exec, vcc
	ds_write2_b32 v3, v4, v110 offset1:1
	v_add_u32_e32 v1, 0x200, v1
	s_mov_b64 exec, s[0:1]
	v_cmp_ge_u32_e32 vcc, v109, v0
	v_or_b32_e32 v4, 0xd00, v129
	v_min_u32_e32 v3, v1, v5
	s_mov_b64 exec, vcc
	ds_write2_b32 v3, v4, v109 offset1:1
	v_add_u32_e32 v1, 0x200, v1
	s_mov_b64 exec, s[0:1]
	v_cmp_ge_u32_e32 vcc, v108, v0
	v_or_b32_e32 v4, 0xd40, v129
	v_min_u32_e32 v3, v1, v5
	s_mov_b64 exec, vcc
	ds_write2_b32 v3, v4, v108 offset1:1
	v_add_u32_e32 v1, 0x200, v1
	s_mov_b64 exec, s[0:1]
	v_cmp_ge_u32_e32 vcc, v107, v0
	v_or_b32_e32 v4, 0xd80, v129
	v_min_u32_e32 v3, v1, v5
	s_mov_b64 exec, vcc
	ds_write2_b32 v3, v4, v107 offset1:1
	v_add_u32_e32 v1, 0x200, v1
	s_mov_b64 exec, s[0:1]
	v_cmp_ge_u32_e32 vcc, v106, v0
	v_or_b32_e32 v4, 0xdc0, v129
	v_min_u32_e32 v3, v1, v5
	s_mov_b64 exec, vcc
	ds_write2_b32 v3, v4, v106 offset1:1
	v_add_u32_e32 v1, 0x200, v1
	s_mov_b64 exec, s[0:1]
	s_cmpk_le_u32 s49, 0x38
	s_cbranch_scc1 .Lp1_done
; #define LAS __attribute__((address_space(3)))
; __device__ __forceinline__ bool dsa2_sampled(LAS unsigned char* wl, const unsigned (&kk)[128], int nreg, int n, int lane) {
;     ...
;     bl = bl < 1u ? 1u : bl; if (bl > bh) bl = bh;
;     int cur = 0; LAS unsigned* pp = (LAS unsigned*)(PRIV + lane);
; #pragma unroll
;     for (int i = 0; i < 128; ++i) { if ((i & ~15) < nreg) { const unsigned k = kk[i];
;             if ((k >> 21) >= bl) { if (cur < 24) { pp[0] = (unsigned)(lane + 64 * i); pp[1] = k; } pp += 128; ++cur; } }
;         __builtin_amdgcn_sched_barrier(0); }
	v_cmp_ge_u32_e32 vcc, v105, v0
	v_or_b32_e32 v4, 0xe00, v129
	v_min_u32_e32 v3, v1, v5
	s_mov_b64 exec, vcc
	ds_write2_b32 v3, v4, v105 offset1:1
	v_add_u32_e32 v1, 0x200, v1
	s_mov_b64 exec, s[0:1]
	v_cmp_ge_u32_e32 vcc, v104, v0
	v_or_b32_e32 v4, 0xe40, v129
	v_min_u32_e32 v3, v1, v5
	s_mov_b64 exec, vcc
	ds_write2_b32 v3, v4, v104 offset1:1
	v_add_u32_e32 v1, 0x200, v1
	s_mov_b64 exec, s[0:1]
	v_cmp_ge_u32_e32 vcc, v103, v0
	v_or_b32_e32 v4, 0xe80, v129
	v_min_u32_e32 v3, v1, v5
	s_mov_b64 exec, vcc
	ds_write2_b32 v3, v4, v103 offset1:1
	v_add_u32_e32 v1, 0x200, v1
	s_mov_b64 exec, s[0:1]
	v_cmp_ge_u32_e32 vcc, v102, v0
	v_or_b32_e32 v4, 0xec0, v129
	v_min_u32_e32 v3, v1, v5
	s_mov_b64 exec, vcc
	ds_write2_b32 v3, v4, v102 offset1:1
	v_add_u32_e32 v1, 0x200, v1
	s_mov_b64 exec, s[0:1]
	v_cmp_ge_u32_e32 vcc, v100, v0
	v_or_b32_e32 v4, 0xf00, v129
	v_min_u32_e32 v3, v1, v5
	s_mov_b64 exec, vcc
	ds_write2_b32 v3, v4, v100 offset1:1
	v_add_u32_e32 v1, 0x200, v1
	s_mov_b64 exec, s[0:1]
	v_cmp_ge_u32_e32 vcc, v98, v0
	v_or_b32_e32 v4, 0xf40, v129
	v_min_u32_e32 v3, v1, v5
	s_mov_b64 exec, vcc
	ds_write2_b32 v3, v4, v98 offset1:1
	v_add_u32_e32 v1, 0x200, v1
	s_mov_b64 exec, s[0:1]
	v_cmp_ge_u32_e32 vcc, v96, v0
	v_or_b32_e32 v4, 0xf80, v129
	v_min_u32_e32 v3, v1, v5
	s_mov_b64 exec, vcc
	ds_write2_b32 v3, v4, v96 offset1:1
	v_add_u32_e32 v1, 0x200, v1
	s_mov_b64 exec, s[0:1]
	v_cmp_ge_u32_e32 vcc, v94, v0
	v_or_b32_e32 v4, 0xfc0, v129
	v_min_u32_e32 v3, v1, v5
	s_mov_b64 exec, vcc
	ds_write2_b32 v3, v4, v94 offset1:1
	v_add_u32_e32 v1, 0x200, v1
	s_mov_b64 exec, s[0:1]
	s_cmpk_le_u32 s49, 0x40
	s_cbranch_scc1 .Lp1_done
	v_cmp_ge_u32_e32 vcc, v101, v0
	v_or_b32_e32 v4, 0x1000, v129
	v_min_u32_e32 v3, v1, v5
	s_mov_b64 exec, vcc
	ds_write2_b32 v3, v4, v101 offset1:1
	v_add_u32_e32 v1, 0x200, v1
	s_mov_b64 exec, s[0:1]
	v_cmp_ge_u32_e32 vcc, v99, v0
	v_or_b32_e32 v4, 0x1040, v129
	v_min_u32_e32 v3, v1, v5
	s_mov_b64 exec, vcc
	ds_write2_b32 v3, v4, v99 offset1:1
	v_add_u32_e32 v1, 0x200, v1
	s_mov_b64 exec, s[0:1]
	v_cmp_ge_u32_e32 vcc, v97, v0
	v_or_b32_e32 v4, 0x1080, v129
	v_min_u32_e32 v3, v1, v5
	s_mov_b64 exec, vcc
	ds_write2_b32 v3, v4, v97 offset1:1
	v_add_u32_e32 v1, 0x200, v1
	s_mov_b64 exec, s[0:1]
	v_cmp_ge_u32_e32 vcc, v95, v0
	v_or_b32_e32 v4, 0x10c0, v129
	v_min_u32_e32 v3, v1, v5
	s_mov_b64 exec, vcc
	ds_write2_b32 v3, v4, v95 offset1:1
	v_add_u32_e32 v1, 0x200, v1
	s_mov_b64 exec, s[0:1]
	v_cmp_ge_u32_e32 vcc, v93, v0
	v_or_b32_e32 v4, 0x1100, v129
	v_min_u32_e32 v3, v1, v5
	s_mov_b64 exec, vcc
	ds_write2_b32 v3, v4, v93 offset1:1
	v_add_u32_e32 v1, 0x200, v1
	s_mov_b64 exec, s[0:1]
	v_cmp_ge_u32_e32 vcc, v92, v0
	v_or_b32_e32 v4, 0x1140, v129
	v_min_u32_e32 v3, v1, v5
	s_mov_b64 exec, vcc
	ds_write2_b32 v3, v4, v92 offset1:1
	v_add_u32_e32 v1, 0x200, v1
	s_mov_b64 exec, s[0:1]
	v_cmp_ge_u32_e32 vcc, v91, v0
	v_or_b32_e32 v4, 0x1180, v129
	v_min_u32_e32 v3, v1, v5
	s_mov_b64 exec, vcc
	ds_write2_b32 v3, v4, v91 offset1:1
	v_add_u32_e32 v1, 0x200, v1
	s_mov_b64 exec, s[0:1]
	v_cmp_ge_u32_e32 vcc, v90, v0
	v_or_b32_e32 v4, 0x11c0, v129
	v_min_u32_e32 v3, v1, v5
	s_mov_b64 exec, vcc
	ds_write2_b32 v3, v4, v90 offset1:1
	v_add_u32_e32 v1, 0x200, v1
	s_mov_b64 exec, s[0:1]
	s_cmpk_le_u32 s49, 0x48
	s_cbranch_scc1 .Lp1_done
	v_cmp_ge_u32_e32 vcc, v89, v0
	v_or_b32_e32 v4, 0x1200, v129
	v_min_u32_e32 v3, v1, v5
	s_mov_b64 exec, vcc
	ds_write2_b32 v3, v4, v89 offset1:1
	v_add_u32_e32 v1, 0x200, v1
	s_mov_b64 exec, s[0:1]
	v_cmp_ge_u32_e32 vcc, v88, v0
	v_or_b32_e32 v4, 0x1240, v129
	v_min_u32_e32 v3, v1, v5
	s_mov_b64 exec, vcc
	ds_write2_b32 v3, v4, v88 offset1:1
	v_add_u32_e32 v1, 0x200, v1
	s_mov_b64 exec, s[0:1]
	v_cmp_ge_u32_e32 vcc, v87, v0
	v_or_b32_e32 v4, 0x1280, v129
	v_min_u32_e32 v3, v1, v5
	s_mov_b64 exec, vcc
	ds_write2_b32 v3, v4, v87 offset1:1
	v_add_u32_e32 v1, 0x200, v1
	s_mov_b64 exec, s[0:1]
	v_cmp_ge_u32_e32 vcc, v86, v0
	v_or_b32_e32 v4, 0x12c0, v129
	v_min_u32_e32 v3, v1, v5
	s_mov_b64 exec, vcc
	ds_write2_b32 v3, v4, v86 offset1:1
	v_add_u32_e32 v1, 0x200, v1
	s_mov_b64 exec, s[0:1]
	v_cmp_ge_u32_e32 vcc, v85, v0
	v_or_b32_e32 v4, 0x1300, v129
	v_min_u32_e32 v3, v1, v5
	s_mov_b64 exec, vcc
	ds_write2_b32 v3, v4, v85 offset1:1
	v_add_u32_e32 v1, 0x200, v1
	s_mov_b64 exec, s[0:1]
	v_cmp_ge_u32_e32 vcc, v84, v0
	v_or_b32_e32 v4, 0x1340, v129
	v_min_u32_e32 v3, v1, v5
	s_mov_b64 exec, vcc
	ds_write2_b32 v3, v4, v84 offset1:1
	v_add_u32_e32 v1, 0x200, v1
	s_mov_b64 exec, s[0:1]
	v_cmp_ge_u32_e32 vcc, v83, v0
	v_or_b32_e32 v4, 0x1380, v129
	v_min_u32_e32 v3, v1, v5
	s_mov_b64 exec, vcc
	ds_write2_b32 v3, v4, v83 offset1:1
	v_add_u32_e32 v1, 0x200, v1
	s_mov_b64 exec, s[0:1]
	v_cmp_ge_u32_e32 vcc, v82, v0
	v_or_b32_e32 v4, 0x13c0, v129
	v_min_u32_e32 v3, v1, v5
	s_mov_b64 exec, vcc
	ds_write2_b32 v3, v4, v82 offset1:1
	v_add_u32_e32 v1, 0x200, v1
	s_mov_b64 exec, s[0:1]
	s_cmpk_le_u32 s49, 0x50
	s_cbranch_scc1 .Lp1_done
; #define LAS __attribute__((address_space(3)))
; __device__ __forceinline__ bool dsa2_sampled(LAS unsigned char* wl, const unsigned (&kk)[128], int nreg, int n, int lane) {
;     ...
;     bl = bl < 1u ? 1u : bl; if (bl > bh) bl = bh;
;     int cur = 0; LAS unsigned* pp = (LAS unsigned*)(PRIV + lane);
; #pragma unroll
;     for (int i = 0; i < 128; ++i) { if ((i & ~15) < nreg) { const unsigned k = kk[i];
;             if ((k >> 21) >= bl) { if (cur < 24) { pp[0] = (unsigned)(lane + 64 * i); pp[1] = k; } pp += 128; ++cur; } }
;         __builtin_amdgcn_sched_barrier(0); }
	v_cmp_ge_u32_e32 vcc, v81, v0
	v_or_b32_e32 v4, 0x1400, v129
	v_min_u32_e32 v3, v1, v5
	s_mov_b64 exec, vcc
	ds_write2_b32 v3, v4, v81 offset1:1
	v_add_u32_e32 v1, 0x200, v1
	s_mov_b64 exec, s[0:1]
	v_cmp_ge_u32_e32 vcc, v80, v0
	v_or_b32_e32 v4, 0x1440, v129
	v_min_u32_e32 v3, v1, v5
	s_mov_b64 exec, vcc
	ds_write2_b32 v3, v4, v80 offset1:1
	v_add_u32_e32 v1, 0x200, v1
	s_mov_b64 exec, s[0:1]
	v_cmp_ge_u32_e32 vcc, v79, v0
	v_or_b32_e32 v4, 0x1480, v129
	v_min_u32_e32 v3, v1, v5
	s_mov_b64 exec, vcc
	ds_write2_b32 v3, v4, v79 offset1:1
	v_add_u32_e32 v1, 0x200, v1
	s_mov_b64 exec, s[0:1]
	v_cmp_ge_u32_e32 vcc, v78, v0
	v_or_b32_e32 v4, 0x14c0, v129
	v_min_u32_e32 v3, v1, v5
	s_mov_b64 exec, vcc
	ds_write2_b32 v3, v4, v78 offset1:1
	v_add_u32_e32 v1, 0x200, v1
	s_mov_b64 exec, s[0:1]
	v_cmp_ge_u32_e32 vcc, v77, v0
	v_or_b32_e32 v4, 0x1500, v129
	v_min_u32_e32 v3, v1, v5
	s_mov_b64 exec, vcc
	ds_write2_b32 v3, v4, v77 offset1:1
	v_add_u32_e32 v1, 0x200, v1
	s_mov_b64 exec, s[0:1]
	v_cmp_ge_u32_e32 vcc, v76, v0
	v_or_b32_e32 v4, 0x1540, v129
	v_min_u32_e32 v3, v1, v5
	s_mov_b64 exec, vcc
	ds_write2_b32 v3, v4, v76 offset1:1
	v_add_u32_e32 v1, 0x200, v1
	s_mov_b64 exec, s[0:1]
	v_cmp_ge_u32_e32 vcc, v75, v0
	v_or_b32_e32 v4, 0x1580, v129
	v_min_u32_e32 v3, v1, v5
	s_mov_b64 exec, vcc
	ds_write2_b32 v3, v4, v75 offset1:1
	v_add_u32_e32 v1, 0x200, v1
	s_mov_b64 exec, s[0:1]
	v_cmp_ge_u32_e32 vcc, v74, v0
	v_or_b32_e32 v4, 0x15c0, v129
	v_min_u32_e32 v3, v1, v5
	s_mov_b64 exec, vcc
	ds_write2_b32 v3, v4, v74 offset1:1
	v_add_u32_e32 v1, 0x200, v1
	s_mov_b64 exec, s[0:1]
	s_cmpk_le_u32 s49, 0x58
	s_cbranch_scc1 .Lp1_done
	v_cmp_ge_u32_e32 vcc, v73, v0
	v_or_b32_e32 v4, 0x1600, v129
	v_min_u32_e32 v3, v1, v5
	s_mov_b64 exec, vcc
	ds_write2_b32 v3, v4, v73 offset1:1
	v_add_u32_e32 v1, 0x200, v1
	s_mov_b64 exec, s[0:1]
	v_cmp_ge_u32_e32 vcc, v72, v0
	v_or_b32_e32 v4, 0x1640, v129
	v_min_u32_e32 v3, v1, v5
	s_mov_b64 exec, vcc
	ds_write2_b32 v3, v4, v72 offset1:1
	v_add_u32_e32 v1, 0x200, v1
	s_mov_b64 exec, s[0:1]
	v_cmp_ge_u32_e32 vcc, v71, v0
	v_or_b32_e32 v4, 0x1680, v129
	v_min_u32_e32 v3, v1, v5
	s_mov_b64 exec, vcc
	ds_write2_b32 v3, v4, v71 offset1:1
	v_add_u32_e32 v1, 0x200, v1
	s_mov_b64 exec, s[0:1]
	v_cmp_ge_u32_e32 vcc, v70, v0
	v_or_b32_e32 v4, 0x16c0, v129
	v_min_u32_e32 v3, v1, v5
	s_mov_b64 exec, vcc
	ds_write2_b32 v3, v4, v70 offset1:1
	v_add_u32_e32 v1, 0x200, v1
	s_mov_b64 exec, s[0:1]
	v_cmp_ge_u32_e32 vcc, v68, v0
	v_or_b32_e32 v4, 0x1700, v129
	v_min_u32_e32 v3, v1, v5
	s_mov_b64 exec, vcc
	ds_write2_b32 v3, v4, v68 offset1:1
	v_add_u32_e32 v1, 0x200, v1
	s_mov_b64 exec, s[0:1]
	v_cmp_ge_u32_e32 vcc, v66, v0
	v_or_b32_e32 v4, 0x1740, v129
	v_min_u32_e32 v3, v1, v5
	s_mov_b64 exec, vcc
	ds_write2_b32 v3, v4, v66 offset1:1
	v_add_u32_e32 v1, 0x200, v1
	s_mov_b64 exec, s[0:1]
	v_cmp_ge_u32_e32 vcc, v64, v0
	v_or_b32_e32 v4, 0x1780, v129
	v_min_u32_e32 v3, v1, v5
	s_mov_b64 exec, vcc
	ds_write2_b32 v3, v4, v64 offset1:1
	v_add_u32_e32 v1, 0x200, v1
	s_mov_b64 exec, s[0:1]
	v_cmp_ge_u32_e32 vcc, v57, v0
	v_or_b32_e32 v4, 0x17c0, v129
	v_min_u32_e32 v3, v1, v5
	s_mov_b64 exec, vcc
	ds_write2_b32 v3, v4, v57 offset1:1
	v_add_u32_e32 v1, 0x200, v1
	s_mov_b64 exec, s[0:1]
	s_cmpk_le_u32 s49, 0x60
	s_cbranch_scc1 .Lp1_done
	v_cmp_ge_u32_e32 vcc, v69, v0
	v_or_b32_e32 v4, 0x1800, v129
	v_min_u32_e32 v3, v1, v5
	s_mov_b64 exec, vcc
	ds_write2_b32 v3, v4, v69 offset1:1
	v_add_u32_e32 v1, 0x200, v1
	s_mov_b64 exec, s[0:1]
	v_cmp_ge_u32_e32 vcc, v67, v0
	v_or_b32_e32 v4, 0x1840, v129
	v_min_u32_e32 v3, v1, v5
	s_mov_b64 exec, vcc
	ds_write2_b32 v3, v4, v67 offset1:1
	v_add_u32_e32 v1, 0x200, v1
	s_mov_b64 exec, s[0:1]
	v_cmp_ge_u32_e32 vcc, v65, v0
	v_or_b32_e32 v4, 0x1880, v129
	v_min_u32_e32 v3, v1, v5
	s_mov_b64 exec, vcc
	ds_write2_b32 v3, v4, v65 offset1:1
	v_add_u32_e32 v1, 0x200, v1
	s_mov_b64 exec, s[0:1]
	v_cmp_ge_u32_e32 vcc, v63, v0
	v_or_b32_e32 v4, 0x18c0, v129
	v_min_u32_e32 v3, v1, v5
	s_mov_b64 exec, vcc
	ds_write2_b32 v3, v4, v63 offset1:1
	v_add_u32_e32 v1, 0x200, v1
	s_mov_b64 exec, s[0:1]
	v_cmp_ge_u32_e32 vcc, v62, v0
	v_or_b32_e32 v4, 0x1900, v129
	v_min_u32_e32 v3, v1, v5
	s_mov_b64 exec, vcc
	ds_write2_b32 v3, v4, v62 offset1:1
	v_add_u32_e32 v1, 0x200, v1
	s_mov_b64 exec, s[0:1]
	v_cmp_ge_u32_e32 vcc, v61, v0
	v_or_b32_e32 v4, 0x1940, v129
	v_min_u32_e32 v3, v1, v5
	s_mov_b64 exec, vcc
	ds_write2_b32 v3, v4, v61 offset1:1
	v_add_u32_e32 v1, 0x200, v1
	s_mov_b64 exec, s[0:1]
	v_cmp_ge_u32_e32 vcc, v60, v0
	v_or_b32_e32 v4, 0x1980, v129
	v_min_u32_e32 v3, v1, v5
	s_mov_b64 exec, vcc
	ds_write2_b32 v3, v4, v60 offset1:1
	v_add_u32_e32 v1, 0x200, v1
	s_mov_b64 exec, s[0:1]
	v_cmp_ge_u32_e32 vcc, v59, v0
	v_or_b32_e32 v4, 0x19c0, v129
	v_min_u32_e32 v3, v1, v5
	s_mov_b64 exec, vcc
	ds_write2_b32 v3, v4, v59 offset1:1
	v_add_u32_e32 v1, 0x200, v1
	s_mov_b64 exec, s[0:1]
	s_cmpk_le_u32 s49, 0x68
	s_cbranch_scc1 .Lp1_done
; #define LAS __attribute__((address_space(3)))
; #define LDS_WAIT() asm volatile("s_waitcnt lgkmcnt(0)" ::: "memory")
; __device__ __forceinline__ int lane_op() { int l = (int)__builtin_amdgcn_mbcnt_hi(~0u, __builtin_amdgcn_mbcnt_lo(~0u, 0u)); asm volatile("" : "+v"(l)); return l; }
; #define SHX(v, m, l) bperm_((l) ^ (m), (v))
; __device__ __forceinline__ bool dsa2_sampled(LAS unsigned char* wl, const unsigned (&kk)[128], int nreg, int n, int lane) {
;     ...
;     bl = bl < 1u ? 1u : bl; if (bl > bh) bl = bh;
;     int cur = 0; LAS unsigned* pp = (LAS unsigned*)(PRIV + lane);
; #pragma unroll
;     for (int i = 0; i < 128; ++i) { if ((i & ~15) < nreg) { const unsigned k = kk[i];
;             if ((k >> 21) >= bl) { if (cur < 24) { pp[0] = (unsigned)(lane + 64 * i); pp[1] = k; } pp += 128; ++cur; } }
;         __builtin_amdgcn_sched_barrier(0); }
;     LDS_WAIT();
;     int mxc = cur; { const int lq_ = lane_op();
; #pragma unroll
;         for (int o = 1; o < 64; o <<= 1) { const int t2 = SHX(mxc, o, lq_); mxc = t2 > mxc ? t2 : mxc; } }
;     mxc = __builtin_amdgcn_readfirstlane(mxc);
;     if (mxc > 24) return false;
;     int A = 0, C = 0;
; #pragma unroll 1
;     for (int s = 0; s < mxc; ++s) { const bool vld = s < cur; const unsigned long long e = vld ? PRIV[s * 64 + lane] : 0ull; const unsigned k = (unsigned)(e >> 32), ix = (unsigned)e;
	v_cmp_ge_u32_e32 vcc, v58, v0
	v_or_b32_e32 v4, 0x1a00, v129
	v_min_u32_e32 v3, v1, v5
	s_mov_b64 exec, vcc
	ds_write2_b32 v3, v4, v58 offset1:1
	v_add_u32_e32 v1, 0x200, v1
	s_mov_b64 exec, s[0:1]
	v_cmp_ge_u32_e32 vcc, v56, v0
	v_or_b32_e32 v4, 0x1a40, v129
	v_min_u32_e32 v3, v1, v5
	s_mov_b64 exec, vcc
	ds_write2_b32 v3, v4, v56 offset1:1
	v_add_u32_e32 v1, 0x200, v1
	s_mov_b64 exec, s[0:1]
	v_cmp_ge_u32_e32 vcc, v55, v0
	v_or_b32_e32 v4, 0x1a80, v129
	v_min_u32_e32 v3, v1, v5
	s_mov_b64 exec, vcc
	ds_write2_b32 v3, v4, v55 offset1:1
	v_add_u32_e32 v1, 0x200, v1
	s_mov_b64 exec, s[0:1]
	v_cmp_ge_u32_e32 vcc, v54, v0
	v_or_b32_e32 v4, 0x1ac0, v129
	v_min_u32_e32 v3, v1, v5
	s_mov_b64 exec, vcc
	ds_write2_b32 v3, v4, v54 offset1:1
	v_add_u32_e32 v1, 0x200, v1
	s_mov_b64 exec, s[0:1]
	v_cmp_ge_u32_e32 vcc, v53, v0
	v_or_b32_e32 v4, 0x1b00, v129
	v_min_u32_e32 v3, v1, v5
	s_mov_b64 exec, vcc
	ds_write2_b32 v3, v4, v53 offset1:1
	v_add_u32_e32 v1, 0x200, v1
	s_mov_b64 exec, s[0:1]
	v_cmp_ge_u32_e32 vcc, v52, v0
	v_or_b32_e32 v4, 0x1b40, v129
	v_min_u32_e32 v3, v1, v5
	s_mov_b64 exec, vcc
	ds_write2_b32 v3, v4, v52 offset1:1
	v_add_u32_e32 v1, 0x200, v1
	s_mov_b64 exec, s[0:1]
	v_cmp_ge_u32_e32 vcc, v51, v0
	v_or_b32_e32 v4, 0x1b80, v129
	v_min_u32_e32 v3, v1, v5
	s_mov_b64 exec, vcc
	ds_write2_b32 v3, v4, v51 offset1:1
	v_add_u32_e32 v1, 0x200, v1
	s_mov_b64 exec, s[0:1]
	v_cmp_ge_u32_e32 vcc, v50, v0
	v_or_b32_e32 v4, 0x1bc0, v129
	v_min_u32_e32 v3, v1, v5
	s_mov_b64 exec, vcc
	ds_write2_b32 v3, v4, v50 offset1:1
	v_add_u32_e32 v1, 0x200, v1
	s_mov_b64 exec, s[0:1]
	s_cmpk_le_u32 s49, 0x70
	s_cbranch_scc1 .Lp1_done
	v_cmp_ge_u32_e32 vcc, v49, v0
	v_or_b32_e32 v4, 0x1c00, v129
	v_min_u32_e32 v3, v1, v5
	s_mov_b64 exec, vcc
	ds_write2_b32 v3, v4, v49 offset1:1
	v_add_u32_e32 v1, 0x200, v1
	s_mov_b64 exec, s[0:1]
	v_cmp_ge_u32_e32 vcc, v48, v0
	v_or_b32_e32 v4, 0x1c40, v129
	v_min_u32_e32 v3, v1, v5
	s_mov_b64 exec, vcc
	ds_write2_b32 v3, v4, v48 offset1:1
	v_add_u32_e32 v1, 0x200, v1
	s_mov_b64 exec, s[0:1]
	v_cmp_ge_u32_e32 vcc, v47, v0
	v_or_b32_e32 v4, 0x1c80, v129
	v_min_u32_e32 v3, v1, v5
	s_mov_b64 exec, vcc
	ds_write2_b32 v3, v4, v47 offset1:1
	v_add_u32_e32 v1, 0x200, v1
	s_mov_b64 exec, s[0:1]
	v_cmp_ge_u32_e32 vcc, v46, v0
	v_or_b32_e32 v4, 0x1cc0, v129
	v_min_u32_e32 v3, v1, v5
	s_mov_b64 exec, vcc
	ds_write2_b32 v3, v4, v46 offset1:1
	v_add_u32_e32 v1, 0x200, v1
	s_mov_b64 exec, s[0:1]
	v_cmp_ge_u32_e32 vcc, v45, v0
	v_or_b32_e32 v4, 0x1d00, v129
	v_min_u32_e32 v3, v1, v5
	s_mov_b64 exec, vcc
	ds_write2_b32 v3, v4, v45 offset1:1
	v_add_u32_e32 v1, 0x200, v1
	s_mov_b64 exec, s[0:1]
	v_cmp_ge_u32_e32 vcc, v44, v0
	v_or_b32_e32 v4, 0x1d40, v129
	v_min_u32_e32 v3, v1, v5
	s_mov_b64 exec, vcc
	ds_write2_b32 v3, v4, v44 offset1:1
	v_add_u32_e32 v1, 0x200, v1
	s_mov_b64 exec, s[0:1]
	v_cmp_ge_u32_e32 vcc, v43, v0
	v_or_b32_e32 v4, 0x1d80, v129
	v_min_u32_e32 v3, v1, v5
	s_mov_b64 exec, vcc
	ds_write2_b32 v3, v4, v43 offset1:1
	v_add_u32_e32 v1, 0x200, v1
	s_mov_b64 exec, s[0:1]
	v_cmp_ge_u32_e32 vcc, v42, v0
	v_or_b32_e32 v4, 0x1dc0, v129
	v_min_u32_e32 v3, v1, v5
	s_mov_b64 exec, vcc
	ds_write2_b32 v3, v4, v42 offset1:1
	v_add_u32_e32 v1, 0x200, v1
	s_mov_b64 exec, s[0:1]
	s_cmpk_le_u32 s49, 0x78
	s_cbranch_scc1 .Lp1_done
	v_cmp_ge_u32_e32 vcc, v41, v0
	v_or_b32_e32 v4, 0x1e00, v129
	v_min_u32_e32 v3, v1, v5
	s_mov_b64 exec, vcc
	ds_write2_b32 v3, v4, v41 offset1:1
	v_add_u32_e32 v1, 0x200, v1
	s_mov_b64 exec, s[0:1]
	v_cmp_ge_u32_e32 vcc, v40, v0
	v_or_b32_e32 v4, 0x1e40, v129
	v_min_u32_e32 v3, v1, v5
	s_mov_b64 exec, vcc
	ds_write2_b32 v3, v4, v40 offset1:1
	v_add_u32_e32 v1, 0x200, v1
	s_mov_b64 exec, s[0:1]
	v_cmp_ge_u32_e32 vcc, v39, v0
	v_or_b32_e32 v4, 0x1e80, v129
	v_min_u32_e32 v3, v1, v5
	s_mov_b64 exec, vcc
	ds_write2_b32 v3, v4, v39 offset1:1
	v_add_u32_e32 v1, 0x200, v1
	s_mov_b64 exec, s[0:1]
	v_cmp_ge_u32_e32 vcc, v38, v0
	v_or_b32_e32 v4, 0x1ec0, v129
	v_min_u32_e32 v3, v1, v5
	s_mov_b64 exec, vcc
	ds_write2_b32 v3, v4, v38 offset1:1
	v_add_u32_e32 v1, 0x200, v1
	s_mov_b64 exec, s[0:1]
	v_cmp_ge_u32_e32 vcc, v37, v0
	v_or_b32_e32 v4, 0x1f00, v129
	v_min_u32_e32 v3, v1, v5
	s_mov_b64 exec, vcc
	ds_write2_b32 v3, v4, v37 offset1:1
	v_add_u32_e32 v1, 0x200, v1
	s_mov_b64 exec, s[0:1]
	v_cmp_ge_u32_e32 vcc, v36, v0
	v_or_b32_e32 v4, 0x1f40, v129
	v_min_u32_e32 v3, v1, v5
	s_mov_b64 exec, vcc
	ds_write2_b32 v3, v4, v36 offset1:1
	v_add_u32_e32 v1, 0x200, v1
	s_mov_b64 exec, s[0:1]
	v_cmp_ge_u32_e32 vcc, v35, v0
	v_or_b32_e32 v4, 0x1f80, v129
	v_min_u32_e32 v3, v1, v5
	s_mov_b64 exec, vcc
	ds_write2_b32 v3, v4, v35 offset1:1
	v_add_u32_e32 v1, 0x200, v1
	s_mov_b64 exec, s[0:1]
	v_cmp_ge_u32_e32 vcc, v32, v0
	v_or_b32_e32 v4, 0x1fc0, v129
	v_min_u32_e32 v3, v1, v5
	s_mov_b64 exec, vcc
	ds_write2_b32 v3, v4, v32 offset1:1
	v_add_u32_e32 v1, 0x200, v1
	s_mov_b64 exec, s[0:1]
.Lp1_done:
	v_sub_u32_e32 v3, v1, v6
	v_lshrrev_b32_e32 v3, 9, v3
	v_mov_b32_e32 v0, v251
	s_waitcnt lgkmcnt(0)
	s_mov_b64 s[0:1], -1
	v_lshlrev_b32_e32 v0, 2, v0
	v_mov_b32_e32 v1, v3
	s_nop 1
	v_max_i32_dpp v1, v1, v1 quad_perm:[1,0,3,2] row_mask:0xf bank_mask:0xf
	s_nop 1
	v_max_i32_dpp v1, v1, v1 quad_perm:[2,3,0,1] row_mask:0xf bank_mask:0xf
	s_nop 1
	v_max_i32_dpp v1, v1, v1 row_half_mirror row_mask:0xf bank_mask:0xf
	s_nop 1
	v_max_i32_dpp v1, v1, v1 row_mirror row_mask:0xf bank_mask:0xf
	v_mov_b32_e32 v0, v1
	v_mov_b32_e32 v4, v1
	s_nop 1
	v_permlane16_swap_b32 v0, v4
	v_max_i32_e32 v1, v0, v4
	v_mov_b32_e32 v0, v1
	v_mov_b32_e32 v4, v1
	s_nop 1
	v_permlane32_swap_b32 v0, v4
	v_max_i32_e32 v0, v0, v4
	s_nop 0
	v_readfirstlane_b32 s12, v0
	s_cmp_gt_i32 s12, 24
	s_cbranch_scc1 .LBB0_1271
	s_mov_b32 s20, 0
	s_cmp_lt_i32 s12, 1
	s_cbranch_scc1 .LBB0_1246
	v_mov_b32_e32 v4, v6
	s_mov_b32 s21, 0
	s_mov_b32 s13, 0
	ds_read_b64 v[186:187], v4
	s_branch .LBB0_1231
